# stack G plus: prologue bias and distance-table loads consumed after the single final vmcnt(0), overlapping the K/V DMA and Q loads
# speedup vs baseline: 1.0058x; 1.0058x over previous
.LBB0_632:
	s_lshl_b32 s0, s40, 1
	s_lshr_b32 s5, s9, 6
	s_add_i32 s5, s5, s0
	s_and_b32 s4, s5, 7
	s_lshl_b32 s0, s4, 2
	v_readlane_b32 s12, v254, 12
	v_mov_b32_e32 v1, s0
	v_readlane_b32 s22, v254, 22
	v_readlane_b32 s23, v254, 23
	v_readfirstlane_b32 s2, v0
	v_readlane_b32 s13, v254, 13
	v_readlane_b32 s14, v254, 14
	v_readlane_b32 s15, v254, 15
	v_readlane_b32 s16, v254, 16
	global_load_dword v101, v1, s[22:23] offset:992
	v_readlane_b32 s17, v254, 17
	v_readlane_b32 s18, v254, 18
	v_readlane_b32 s19, v254, 19
	v_readlane_b32 s20, v254, 20
	v_readlane_b32 s21, v254, 21
	v_readlane_b32 s24, v254, 24
	v_readlane_b32 s25, v254, 25
	v_readlane_b32 s26, v254, 26
	v_readlane_b32 s27, v254, 27
	s_mov_b64 s[0:1], exec
	v_readlane_b32 s10, v255, 1
	v_readlane_b32 s11, v255, 2
	s_and_b64 s[10:11], s[0:1], s[10:11]
	s_mov_b64 exec, s[10:11]
	s_cbranch_execz .Lpro_nold
	v_or_b32_e32 v2, s4, v215
	v_lshl_add_u64 v[4:5], v[2:3], 2, s[22:23]
	global_load_dword v100, v[4:5], off

.LBB0_634:
	s_or_b64 exec, exec, s[0:1]
	s_not_b32 s0, s9
	s_bfe_u32 s73, s2, 0x20006
	s_lshl_b32 s0, s0, 7
	s_ashr_i32 s10, s5, 3
	s_and_b32 s53, s0, 0x1f80
	s_lshl_b32 s0, s73, 5
	s_or_b32 s9, s0, s53
	s_and_b32 s0, s2, 0x3fffffc0
	s_ashr_i32 s11, s10, 31
	v_or_b32_e32 v1, s9, v180
	s_lshl_b32 s0, s0, 2
	s_lshl_b64 s[54:55], s[10:11], 13
	s_add_i32 s95, s0, 0
	v_or_b32_e32 v1, s54, v1
	v_mov_b64_e32 v[4:5], s[88:89]
	s_movk_i32 s0, 0x6880
	v_mad_u64_u32 v[4:5], s[0:1], v1, s0, v[4:5]
	s_lshr_b32 s13, s2, 8
	v_mad_i32_i24 v5, s55, v227, v5
	s_lshl_b32 s42, s4, 8
	v_lshl_add_u64 v[4:5], v[4:5], 0, s[42:43]
	s_lshl_b32 s0, s13, 7
	s_mov_b32 s1, s43
	s_lshr_b32 s12, s2, 6
	s_add_i32 s95, s95, 0x20800
	s_lshl_b32 s72, s4, 7
	v_lshl_add_u64 v[4:5], v[4:5], 0, s[0:1]
	s_mul_i32 s1, s10, 0xd100000
	s_mul_hi_i32 s14, s10, 0xd100000
	s_add_u32 s4, s88, s1
	s_addc_u32 s5, s89, s14
	s_add_u32 s4, s4, s42
	s_addc_u32 s5, s5, 0
	s_lshl_b32 s15, s12, 3
	s_lshr_b32 s10, s2, 4
	v_or_b32_e32 v6, s15, v193
	s_and_b32 s16, s10, 4
	v_mad_u64_u32 v[6:7], s[10:11], v6, s94, v[200:201]
	v_or_b32_e32 v7, s15, v221
	v_bitop3_b32 v1, s15, v228, v218 bitop3:0xc8
	v_mad_u64_u32 v[8:9], s[10:11], v7, s94, v[202:203]
	v_mov_b32_e32 v7, v3
	v_or3_b32 v2, v219, v1, s16
	s_lshl_b32 s10, s12, 11
	v_lshlrev_b64 v[6:7], 1, v[6:7]
	v_mul_lo_u32 v2, v2, s94
	v_lshl_add_u64 v[12:13], s[4:5], 0, v[6:7]
	s_mov_b64 s[18:19], 0x800
	s_add_i32 s52, s10, 0
	v_or_b32_e32 v2, v2, v223
	v_lshl_add_u64 v[12:13], v[12:13], 0, s[18:19]
	s_mov_b32 m0, s52
	s_mov_b64 s[10:11], 0x1000
	global_load_lds_dwordx4 v[12:13], off
	v_lshlrev_b64 v[12:13], 1, v[2:3]
	v_lshl_add_u64 v[14:15], s[4:5], 0, v[12:13]
	v_mov_b32_e32 v9, v3
	v_lshl_add_u64 v[16:17], v[14:15], 0, s[10:11]
	s_add_i32 m0, s52, 0x4000
	v_lshlrev_b64 v[8:9], 1, v[8:9]
	global_load_lds_dwordx4 v[16:17], off
	v_lshl_add_u64 v[16:17], s[4:5], 0, v[8:9]
	v_lshl_add_u64 v[16:17], v[16:17], 0, s[18:19]
	s_add_i32 m0, s52, 0x400
	s_addk_i32 s53, 0x80
	global_load_lds_dwordx4 v[16:17], off
	s_mov_b64 s[10:11], 0x1080
	s_add_i32 m0, s52, 0x4400
	v_lshl_add_u64 v[14:15], v[14:15], 0, s[10:11]
	s_add_u32 s10, s4, 0x1a2800
	s_addc_u32 s11, s5, 0
	s_add_u32 s4, s4, 0x1a3000
	global_load_lds_dwordx4 v[14:15], off
	s_addc_u32 s5, s5, 0
	v_lshl_add_u64 v[6:7], s[10:11], 0, v[6:7]
	s_add_i32 m0, s52, 0x8000
	v_add_u32_e32 v10, 64, v2
	global_load_lds_dwordx4 v[6:7], off
	v_lshl_add_u64 v[6:7], s[4:5], 0, v[12:13]
	s_add_i32 m0, s52, 0xc000
	v_mov_b32_e32 v11, v3
	global_load_lds_dwordx4 v[6:7], off
	v_lshl_add_u64 v[6:7], s[10:11], 0, v[8:9]
	s_add_i32 m0, s52, 0x8400
	v_lshlrev_b32_e32 v2, 1, v182
	global_load_lds_dwordx4 v[6:7], off
	v_lshl_add_u64 v[6:7], v[10:11], 1, s[4:5]
	s_add_i32 m0, s52, 0xc400
	v_lshl_add_u64 v[4:5], v[4:5], 0, v[2:3]
	global_load_lds_dwordx4 v[6:7], off
	global_load_dwordx4 v[132:135], v[4:5], off
	global_load_dwordx4 v[136:139], v[4:5], off offset:32
	global_load_dwordx4 v[140:143], v[4:5], off offset:64
	global_load_dwordx4 v[144:147], v[4:5], off offset:96
	s_lshr_b32 s76, s53, 6
	s_cmp_eq_u32 s13, 1
	s_cselect_b64 s[56:57], -1, 0
	s_cmpk_lt_u32 s2, 0x100
	v_or_b32_e32 v2, s0, v183
	s_cselect_b64 s[58:59], -1, 0
	v_bitop3_b32 v234, s0, v186, v183 bitop3:0x36
	s_movk_i32 s0, 0x60
	s_sub_i32 s77, 0xb0, s9
	s_or_b32 s2, s1, s42
	v_add3_u32 v1, v219, v1, s16
	v_bitop3_b32 v237, v2, v186, s0 bitop3:0x36
	v_mul_lo_u32 v1, v1, s94
	s_add_u32 s0, s92, s2
	v_bitop3_b32 v235, v2, v186, 32 bitop3:0x36
	v_bitop3_b32 v236, v2, v186, 64 bitop3:0x36
	v_or_b32_e32 v2, v223, v1
	s_addc_u32 s1, s93, s14
	v_lshl_add_u64 v[206:207], v[2:3], 1, s[0:1]
	s_mul_i32 s12, s12, 0x1a200
	s_add_u32 s0, s84, s2
	v_add_u32_e32 v2, s12, v224
	s_addc_u32 s1, s97, s14
	v_lshl_add_u64 v[208:209], v[2:3], 1, s[0:1]
	v_add_u32_e32 v2, s12, v225
	v_mov_b32_e32 v16, v3
	v_mov_b32_e32 v17, v3
	v_lshl_add_u64 v[210:211], v[2:3], 1, s[0:1]
	v_mov_b32_e32 v2, v3
	v_mov_b32_e32 v4, v3
	v_mov_b32_e32 v5, v3
	v_mov_b32_e32 v6, v3
	v_mov_b32_e32 v7, v3
	v_mov_b32_e32 v8, v3
	v_mov_b32_e32 v9, v3
	v_mov_b32_e32 v10, v3
	v_mov_b32_e32 v12, v3
	v_mov_b32_e32 v13, v3
	v_mov_b32_e32 v14, v3
	v_mov_b32_e32 v15, v3
	v_mov_b64_e32 v[66:67], v[16:17]
	v_mov_b64_e32 v[50:51], v[16:17]
	v_mov_b64_e32 v[34:35], v[16:17]
	v_mov_b64_e32 v[64:65], v[14:15]
	v_mov_b64_e32 v[62:63], v[12:13]
	v_mov_b64_e32 v[60:61], v[10:11]
	v_mov_b64_e32 v[58:59], v[8:9]
	v_mov_b64_e32 v[56:57], v[6:7]
	v_mov_b64_e32 v[54:55], v[4:5]
	v_mov_b64_e32 v[52:53], v[2:3]
	v_mov_b64_e32 v[48:49], v[14:15]
	v_mov_b64_e32 v[46:47], v[12:13]
	v_mov_b64_e32 v[44:45], v[10:11]
	v_mov_b64_e32 v[42:43], v[8:9]
	v_mov_b64_e32 v[40:41], v[6:7]
	v_mov_b64_e32 v[38:39], v[4:5]
	v_mov_b64_e32 v[36:37], v[2:3]
	v_mov_b64_e32 v[32:33], v[14:15]
	v_mov_b64_e32 v[30:31], v[12:13]
	v_mov_b64_e32 v[28:29], v[10:11]
	v_mov_b64_e32 v[26:27], v[8:9]
	v_mov_b64_e32 v[24:25], v[6:7]
	v_mov_b64_e32 v[22:23], v[4:5]
	v_mov_b64_e32 v[20:21], v[2:3]
	v_mov_b64_e32 v[18:19], v[16:17]
	s_mov_b32 s68, 2
	v_lshl_add_u32 v232, v180, 2, s95
	v_add_u32_e32 v238, s9, v226
	s_mov_b32 s42, 0
	v_mov_b32_e32 v233, 0
	s_mov_b32 s4, 0x10000
	s_mov_b64 s[60:61], 0
	v_mov_b32_e32 v84, 0
	v_mov_b32_e32 v85, 0
	v_mov_b32_e32 v86, 0
	v_mov_b32_e32 v87, 0
	v_mov_b32_e32 v88, 0
	v_mov_b32_e32 v89, 0
	v_mov_b32_e32 v90, 0
	v_mov_b32_e32 v91, 0
	v_mov_b32_e32 v92, 0
	v_mov_b32_e32 v93, 0
	v_mov_b32_e32 v94, 0
	v_mov_b32_e32 v95, 0
	v_mov_b32_e32 v96, 0
	v_mov_b32_e32 v97, 0
	v_mov_b32_e32 v98, 0
	v_mov_b32_e32 v99, 0
	v_mov_b64_e32 v[16:17], v[14:15]
	v_mov_b64_e32 v[14:15], v[12:13]
	v_mov_b64_e32 v[12:13], v[10:11]
	v_mov_b64_e32 v[10:11], v[8:9]
	v_mov_b64_e32 v[8:9], v[6:7]
	v_mov_b64_e32 v[6:7], v[4:5]
	v_mov_b64_e32 v[4:5], v[2:3]
	s_waitcnt vmcnt(0)
	v_mul_f32_e32 v68, 0x3fb8aa3b, v101
	v_mov_b32_e32 v69, v68
	v_mov_b32_e32 v70, v68
	v_mov_b32_e32 v71, v68
	v_mov_b32_e32 v72, v68
	v_mov_b32_e32 v73, v68
	v_mov_b32_e32 v74, v68
	v_mov_b32_e32 v75, v68
	v_mov_b32_e32 v76, v68
	v_mov_b32_e32 v77, v68
	v_mov_b32_e32 v78, v68
	v_mov_b32_e32 v79, v68
	v_mov_b32_e32 v80, v68
	v_mov_b32_e32 v81, v68
	v_mov_b32_e32 v82, v68
	v_mov_b32_e32 v83, v68
	s_mov_b64 s[0:1], exec
	v_readlane_b32 s10, v255, 1
	v_readlane_b32 s11, v255, 2
	s_and_b64 s[10:11], s[0:1], s[10:11]
	s_mov_b64 exec, s[10:11]
	s_cbranch_execz .Lpro_nodt
	v_fma_f32 v1, v100, s80, -v68
	ds_write_b32 v217, v1
.Lpro_nodt:
	s_mov_b64 exec, s[0:1]
	s_waitcnt lgkmcnt(0)
	s_and_b64 s[0:1], s[56:57], exec
	s_cbranch_scc0 .Lsp_skip
	s_setprio 1
